# adaLN prologue: the 16 silu(c) loads issued together instead of one dependent round trip per loop trip
# speedup vs baseline: 1.0024x; 1.0023x over previous
.LBB0_9:
	s_mov_b64 s[100:101], 0x1000
	global_load_dword v20, v[2:3], off
	global_load_dword v21, v[2:3], off offset:2048
	v_lshl_add_u64 v[2:3], v[2:3], 0, s[100:101]
	global_load_dword v22, v[2:3], off
	global_load_dword v23, v[2:3], off offset:2048
	v_lshl_add_u64 v[2:3], v[2:3], 0, s[100:101]
	global_load_dword v24, v[2:3], off
	global_load_dword v25, v[2:3], off offset:2048
	v_lshl_add_u64 v[2:3], v[2:3], 0, s[100:101]
	global_load_dword v26, v[2:3], off
	global_load_dword v27, v[2:3], off offset:2048
	v_lshl_add_u64 v[2:3], v[2:3], 0, s[100:101]
	global_load_dword v28, v[2:3], off
	global_load_dword v29, v[2:3], off offset:2048
	v_lshl_add_u64 v[2:3], v[2:3], 0, s[100:101]
	global_load_dword v30, v[2:3], off
	global_load_dword v31, v[2:3], off offset:2048
	v_lshl_add_u64 v[2:3], v[2:3], 0, s[100:101]
	global_load_dword v32, v[2:3], off
	global_load_dword v33, v[2:3], off offset:2048
	v_lshl_add_u64 v[2:3], v[2:3], 0, s[100:101]
	global_load_dword v34, v[2:3], off
	global_load_dword v35, v[2:3], off offset:2048
	s_waitcnt vmcnt(15)
	v_mul_f32_e32 v6, 0xbfb8aa3b, v20
	v_exp_f32_e32 v6, v6
	s_nop 0
	v_add_f32_e32 v6, 1.0, v6
	v_div_scale_f32 v7, s[10:11], v6, v6, v20
	v_rcp_f32_e32 v8, v7
	v_div_scale_f32 v9, vcc, v20, v6, v20
	v_fma_f32 v10, -v7, v8, 1.0
	v_fmac_f32_e32 v8, v10, v8
	v_mul_f32_e32 v10, v9, v8
	v_fma_f32 v11, -v7, v10, v9
	v_fmac_f32_e32 v10, v11, v8
	v_fma_f32 v7, -v7, v10, v9
	v_div_fmas_f32 v7, v7, v8, v10
	v_div_fixup_f32 v5, v7, v6, v20
	ds_write_b32 v4, v5
	s_waitcnt vmcnt(14)
	v_mul_f32_e32 v6, 0xbfb8aa3b, v21
	v_exp_f32_e32 v6, v6
	s_nop 0
	v_add_f32_e32 v6, 1.0, v6
	v_div_scale_f32 v7, s[10:11], v6, v6, v21
	v_rcp_f32_e32 v8, v7
	v_div_scale_f32 v9, vcc, v21, v6, v21
	v_fma_f32 v10, -v7, v8, 1.0
	v_fmac_f32_e32 v8, v10, v8
	v_mul_f32_e32 v10, v9, v8
	v_fma_f32 v11, -v7, v10, v9
	v_fmac_f32_e32 v10, v11, v8
	v_fma_f32 v7, -v7, v10, v9
	v_div_fmas_f32 v7, v7, v8, v10
	v_div_fixup_f32 v5, v7, v6, v21
	ds_write_b32 v4, v5 offset:2048
	s_waitcnt vmcnt(13)
	v_mul_f32_e32 v6, 0xbfb8aa3b, v22
	v_exp_f32_e32 v6, v6
	s_nop 0
	v_add_f32_e32 v6, 1.0, v6
	v_div_scale_f32 v7, s[10:11], v6, v6, v22
	v_rcp_f32_e32 v8, v7
	v_div_scale_f32 v9, vcc, v22, v6, v22
	v_fma_f32 v10, -v7, v8, 1.0
	v_fmac_f32_e32 v8, v10, v8
	v_mul_f32_e32 v10, v9, v8
	v_fma_f32 v11, -v7, v10, v9
	v_fmac_f32_e32 v10, v11, v8
	v_fma_f32 v7, -v7, v10, v9
	v_div_fmas_f32 v7, v7, v8, v10
	v_div_fixup_f32 v5, v7, v6, v22
	ds_write_b32 v4, v5 offset:4096
	s_waitcnt vmcnt(12)
	v_mul_f32_e32 v6, 0xbfb8aa3b, v23
	v_exp_f32_e32 v6, v6
	s_nop 0
	v_add_f32_e32 v6, 1.0, v6
	v_div_scale_f32 v7, s[10:11], v6, v6, v23
	v_rcp_f32_e32 v8, v7
	v_div_scale_f32 v9, vcc, v23, v6, v23
	v_fma_f32 v10, -v7, v8, 1.0
	v_fmac_f32_e32 v8, v10, v8
	v_mul_f32_e32 v10, v9, v8
	v_fma_f32 v11, -v7, v10, v9
	v_fmac_f32_e32 v10, v11, v8
	v_fma_f32 v7, -v7, v10, v9
	v_div_fmas_f32 v7, v7, v8, v10
	v_div_fixup_f32 v5, v7, v6, v23
	ds_write_b32 v4, v5 offset:6144
	s_waitcnt vmcnt(11)
	v_mul_f32_e32 v6, 0xbfb8aa3b, v24
	v_exp_f32_e32 v6, v6
	s_nop 0
	v_add_f32_e32 v6, 1.0, v6
	v_div_scale_f32 v7, s[10:11], v6, v6, v24
	v_rcp_f32_e32 v8, v7
	v_div_scale_f32 v9, vcc, v24, v6, v24
	v_fma_f32 v10, -v7, v8, 1.0
	v_fmac_f32_e32 v8, v10, v8
	v_mul_f32_e32 v10, v9, v8
	v_fma_f32 v11, -v7, v10, v9
	v_fmac_f32_e32 v10, v11, v8
	v_fma_f32 v7, -v7, v10, v9
	v_div_fmas_f32 v7, v7, v8, v10
	v_div_fixup_f32 v5, v7, v6, v24
	ds_write_b32 v4, v5 offset:8192
	s_waitcnt vmcnt(10)
	v_mul_f32_e32 v6, 0xbfb8aa3b, v25
	v_exp_f32_e32 v6, v6
	s_nop 0
	v_add_f32_e32 v6, 1.0, v6
	v_div_scale_f32 v7, s[10:11], v6, v6, v25
	v_rcp_f32_e32 v8, v7
	v_div_scale_f32 v9, vcc, v25, v6, v25
	v_fma_f32 v10, -v7, v8, 1.0
	v_fmac_f32_e32 v8, v10, v8
	v_mul_f32_e32 v10, v9, v8
	v_fma_f32 v11, -v7, v10, v9
	v_fmac_f32_e32 v10, v11, v8
	v_fma_f32 v7, -v7, v10, v9
	v_div_fmas_f32 v7, v7, v8, v10
	v_div_fixup_f32 v5, v7, v6, v25
	ds_write_b32 v4, v5 offset:10240
	s_waitcnt vmcnt(9)
	v_mul_f32_e32 v6, 0xbfb8aa3b, v26
	v_exp_f32_e32 v6, v6
	s_nop 0
	v_add_f32_e32 v6, 1.0, v6
	v_div_scale_f32 v7, s[10:11], v6, v6, v26
	v_rcp_f32_e32 v8, v7
	v_div_scale_f32 v9, vcc, v26, v6, v26
	v_fma_f32 v10, -v7, v8, 1.0
	v_fmac_f32_e32 v8, v10, v8
	v_mul_f32_e32 v10, v9, v8
	v_fma_f32 v11, -v7, v10, v9
	v_fmac_f32_e32 v10, v11, v8
	v_fma_f32 v7, -v7, v10, v9
	v_div_fmas_f32 v7, v7, v8, v10
	v_div_fixup_f32 v5, v7, v6, v26
	ds_write_b32 v4, v5 offset:12288
	s_waitcnt vmcnt(8)
	v_mul_f32_e32 v6, 0xbfb8aa3b, v27
	v_exp_f32_e32 v6, v6
	s_nop 0
	v_add_f32_e32 v6, 1.0, v6
	v_div_scale_f32 v7, s[10:11], v6, v6, v27
	v_rcp_f32_e32 v8, v7
	v_div_scale_f32 v9, vcc, v27, v6, v27
	v_fma_f32 v10, -v7, v8, 1.0
	v_fmac_f32_e32 v8, v10, v8
	v_mul_f32_e32 v10, v9, v8
	v_fma_f32 v11, -v7, v10, v9
	v_fmac_f32_e32 v10, v11, v8
	v_fma_f32 v7, -v7, v10, v9
	v_div_fmas_f32 v7, v7, v8, v10
	v_div_fixup_f32 v5, v7, v6, v27
	ds_write_b32 v4, v5 offset:14336
	s_waitcnt vmcnt(7)
	v_mul_f32_e32 v6, 0xbfb8aa3b, v28
	v_exp_f32_e32 v6, v6
	s_nop 0
	v_add_f32_e32 v6, 1.0, v6
	v_div_scale_f32 v7, s[10:11], v6, v6, v28
	v_rcp_f32_e32 v8, v7
	v_div_scale_f32 v9, vcc, v28, v6, v28
	v_fma_f32 v10, -v7, v8, 1.0
	v_fmac_f32_e32 v8, v10, v8
	v_mul_f32_e32 v10, v9, v8
	v_fma_f32 v11, -v7, v10, v9
	v_fmac_f32_e32 v10, v11, v8
	v_fma_f32 v7, -v7, v10, v9
	v_div_fmas_f32 v7, v7, v8, v10
	v_div_fixup_f32 v5, v7, v6, v28
	ds_write_b32 v4, v5 offset:16384
	s_waitcnt vmcnt(6)
	v_mul_f32_e32 v6, 0xbfb8aa3b, v29
	v_exp_f32_e32 v6, v6
	s_nop 0
	v_add_f32_e32 v6, 1.0, v6
	v_div_scale_f32 v7, s[10:11], v6, v6, v29
	v_rcp_f32_e32 v8, v7
	v_div_scale_f32 v9, vcc, v29, v6, v29
	v_fma_f32 v10, -v7, v8, 1.0
	v_fmac_f32_e32 v8, v10, v8
	v_mul_f32_e32 v10, v9, v8
	v_fma_f32 v11, -v7, v10, v9
	v_fmac_f32_e32 v10, v11, v8
	v_fma_f32 v7, -v7, v10, v9
	v_div_fmas_f32 v7, v7, v8, v10
	v_div_fixup_f32 v5, v7, v6, v29
	ds_write_b32 v4, v5 offset:18432
	s_waitcnt vmcnt(5)
	v_mul_f32_e32 v6, 0xbfb8aa3b, v30
	v_exp_f32_e32 v6, v6
	s_nop 0
	v_add_f32_e32 v6, 1.0, v6
	v_div_scale_f32 v7, s[10:11], v6, v6, v30
	v_rcp_f32_e32 v8, v7
	v_div_scale_f32 v9, vcc, v30, v6, v30
	v_fma_f32 v10, -v7, v8, 1.0
	v_fmac_f32_e32 v8, v10, v8
	v_mul_f32_e32 v10, v9, v8
	v_fma_f32 v11, -v7, v10, v9
	v_fmac_f32_e32 v10, v11, v8
	v_fma_f32 v7, -v7, v10, v9
	v_div_fmas_f32 v7, v7, v8, v10
	v_div_fixup_f32 v5, v7, v6, v30
	ds_write_b32 v4, v5 offset:20480
	s_waitcnt vmcnt(4)
	v_mul_f32_e32 v6, 0xbfb8aa3b, v31
	v_exp_f32_e32 v6, v6
	s_nop 0
	v_add_f32_e32 v6, 1.0, v6
	v_div_scale_f32 v7, s[10:11], v6, v6, v31
	v_rcp_f32_e32 v8, v7
	v_div_scale_f32 v9, vcc, v31, v6, v31
	v_fma_f32 v10, -v7, v8, 1.0
	v_fmac_f32_e32 v8, v10, v8
	v_mul_f32_e32 v10, v9, v8
	v_fma_f32 v11, -v7, v10, v9
	v_fmac_f32_e32 v10, v11, v8
	v_fma_f32 v7, -v7, v10, v9
	v_div_fmas_f32 v7, v7, v8, v10
	v_div_fixup_f32 v5, v7, v6, v31
	ds_write_b32 v4, v5 offset:22528
	s_waitcnt vmcnt(3)
	v_mul_f32_e32 v6, 0xbfb8aa3b, v32
	v_exp_f32_e32 v6, v6
	s_nop 0
	v_add_f32_e32 v6, 1.0, v6
	v_div_scale_f32 v7, s[10:11], v6, v6, v32
	v_rcp_f32_e32 v8, v7
	v_div_scale_f32 v9, vcc, v32, v6, v32
	v_fma_f32 v10, -v7, v8, 1.0
	v_fmac_f32_e32 v8, v10, v8
	v_mul_f32_e32 v10, v9, v8
	v_fma_f32 v11, -v7, v10, v9
	v_fmac_f32_e32 v10, v11, v8
	v_fma_f32 v7, -v7, v10, v9
	v_div_fmas_f32 v7, v7, v8, v10
	v_div_fixup_f32 v5, v7, v6, v32
	ds_write_b32 v4, v5 offset:24576
	s_waitcnt vmcnt(2)
	v_mul_f32_e32 v6, 0xbfb8aa3b, v33
	v_exp_f32_e32 v6, v6
	s_nop 0
	v_add_f32_e32 v6, 1.0, v6
	v_div_scale_f32 v7, s[10:11], v6, v6, v33
	v_rcp_f32_e32 v8, v7
	v_div_scale_f32 v9, vcc, v33, v6, v33
	v_fma_f32 v10, -v7, v8, 1.0
	v_fmac_f32_e32 v8, v10, v8
	v_mul_f32_e32 v10, v9, v8
	v_fma_f32 v11, -v7, v10, v9
	v_fmac_f32_e32 v10, v11, v8
	v_fma_f32 v7, -v7, v10, v9
	v_div_fmas_f32 v7, v7, v8, v10
	v_div_fixup_f32 v5, v7, v6, v33
	ds_write_b32 v4, v5 offset:26624
	s_waitcnt vmcnt(1)
	v_mul_f32_e32 v6, 0xbfb8aa3b, v34
	v_exp_f32_e32 v6, v6
	s_nop 0
	v_add_f32_e32 v6, 1.0, v6
	v_div_scale_f32 v7, s[10:11], v6, v6, v34
	v_rcp_f32_e32 v8, v7
	v_div_scale_f32 v9, vcc, v34, v6, v34
	v_fma_f32 v10, -v7, v8, 1.0
	v_fmac_f32_e32 v8, v10, v8
	v_mul_f32_e32 v10, v9, v8
	v_fma_f32 v11, -v7, v10, v9
	v_fmac_f32_e32 v10, v11, v8
	v_fma_f32 v7, -v7, v10, v9
	v_div_fmas_f32 v7, v7, v8, v10
	v_div_fixup_f32 v5, v7, v6, v34
	ds_write_b32 v4, v5 offset:28672
	s_waitcnt vmcnt(0)
	v_mul_f32_e32 v6, 0xbfb8aa3b, v35
	v_exp_f32_e32 v6, v6
	s_nop 0
	v_add_f32_e32 v6, 1.0, v6
	v_div_scale_f32 v7, s[10:11], v6, v6, v35
	v_rcp_f32_e32 v8, v7
	v_div_scale_f32 v9, vcc, v35, v6, v35
	v_fma_f32 v10, -v7, v8, 1.0
	v_fmac_f32_e32 v8, v10, v8
	v_mul_f32_e32 v10, v9, v8
	v_fma_f32 v11, -v7, v10, v9
	v_fmac_f32_e32 v10, v11, v8
	v_fma_f32 v7, -v7, v10, v9
	v_div_fmas_f32 v7, v7, v8, v10
	v_div_fixup_f32 v5, v7, v6, v35
	ds_write_b32 v4, v5 offset:30720
	s_or_b64 exec, exec, s[0:1]
	s_cmpk_lt_i32 s33, 0xc0
	s_cselect_b64 s[10:11], -1, 0
	s_cmpk_gt_i32 s33, 0xbf
	s_mov_b32 s2, 5
	s_waitcnt lgkmcnt(0)
	s_barrier
	s_cbranch_scc1 .LBB0_24
	v_lshrrev_b32_e32 v8, 6, v178
	v_and_b32_e32 v54, 63, v178
	v_mul_u32_u24_e32 v2, 0x3000, v8
	v_or_b32_e32 v55, v2, v54
	v_lshrrev_b32_e32 v2, 9, v178
	v_sub_u32_e32 v2, 0, v2
	v_and_b32_e32 v56, 15, v2
	v_lshrrev_b32_e32 v2, 4, v178
	v_mul_hi_u32_u24_e32 v5, 0xc000, v2
	v_mul_u32_u24_e32 v4, 0xc000, v2
	v_and_b32_e32 v2, 15, v178
	v_lshlrev_b32_e32 v6, 4, v2
	v_mov_b32_e32 v2, 0
	s_movk_i32 s0, 0x100
	v_mov_b32_e32 v7, v2
	v_or_b32_e32 v4, v4, v6
	v_cmp_gt_u32_e64 s[2:3], s0, v178
	v_lshl_add_u64 v[24:25], s[16:17], 0, v[4:5]
	v_lshl_add_u64 v[4:5], s[16:17], 0, v[6:7]
	s_mov_b64 s[0:1], 0xc00000
	v_lshl_add_u64 v[26:27], v[4:5], 0, s[0:1]
	v_lshlrev_b32_e32 v4, 4, v178
	v_and_b32_e32 v4, 0x3c0, v4
	v_and_b32_e32 v9, 3, v178
	v_lshl_add_u32 v4, v8, 4, v4
	v_lshrrev_b32_e32 v1, 4, v178
	v_lshl_or_b32 v4, v9, 2, v4
	v_lshlrev_b32_e32 v3, 6, v178
	v_lshlrev_b32_e32 v57, 2, v1
	v_add_u32_e32 v4, 0x100, v4
	v_cmp_ne_u32_e64 s[4:5], 0, v56
	v_add_u32_e32 v58, 0x100, v57
	s_mov_b32 s34, 0xc000
	s_lshl_b32 s24, s33, 6
	v_add_u32_e32 v59, 0x8000, v4
	s_mov_b64 s[16:17], 0x180000
	s_mov_b32 s35, 0xff580000
	s_mov_b32 s36, 0xff700000
	s_mov_b32 s37, 0xff880000
	s_mov_b32 s38, 0xffa00000
	s_mov_b32 s39, 0xffb80000
	s_mov_b32 s40, 0xffd00000
	s_mov_b32 s41, 0xffe80000
	s_mov_b32 s42, 0x180000
	s_mov_b32 s43, 0x300000
	s_mov_b32 s44, 0x480000
	s_mov_b32 s45, 0x600000
	s_mov_b32 s46, 0x780000
	s_mov_b32 s47, 0x900000
	s_mov_b32 s48, 0xa80000
	s_mov_b64 s[26:27], 0x1800000
	s_movk_i32 s49, 0x5ff
	v_add_u32_e32 v60, 0x100, v3
	s_mov_b32 s50, s33
	s_branch .LBB0_13
